# vaccH: the 128 KiB LDS table slice is loaded by LDS-DMA from waves 1..7 while they wait in the pw->vaccH grid barrier (was: 16 loads + 16 ds_writes per thread after it)
# baseline (speedup 1.0000x reference)
; #define LAS __attribute__((address_space(3)))
; __device__ __forceinline__ unsigned xb_ld(unsigned* p)              { return __hip_atomic_load(p, __ATOMIC_RELAXED, __HIP_MEMORY_SCOPE_AGENT); }
; #define XB_SPIN(cond, bar) do { unsigned _sp = 0; while (cond) { __builtin_amdgcn_s_sleep(1); \
;     if ((++_sp & 255u) == 0u) { if (xb_ld(&(bar)[XB_TMO])) break; if (_sp > XB_SPIN_CAP) { atomicAdd(&(bar)[XB_TMO], 1u); break; } } } } while (0)
; __device__ __forceinline__ void xcd_barrier(const XcdBarrier& b) {
;     ...
;             XB_SPIN(xb_ld(&bar[XB_XGEN(b.x)]) == gen, bar);
;             __builtin_amdgcn_fence(__ATOMIC_ACQUIRE, "agent");
;             asm volatile("s_waitcnt vmcnt(0)" ::: "memory");
;         }
;     }
;     __syncthreads();
; template <bool RUN_L = true, bool RUN_G = true, bool DRY = false>
; __device__ __forceinline__ void phase_vaccH(unsigned char* ws, LAS unsigned char* lds, int layer, int G) {
;     ...
;     for (int cg = blockIdx.x; cg < NGRP; cg += G) {
;         __syncthreads();
;         { const u32x4* src = (const u32x4*)(pvl + (size_t)cg * (NEXP * 8)) + tid; u32x4 t_[16];
; #pragma unroll
;           for (int i = 0; i < 16; ++i) t_[i] = src[512 * i];
; #pragma unroll
;           for (int i = 0; i < 16; ++i) ((LAS u32x4*)lds)[tid + 512 * i] = t_[i]; }
.LBB0_1227:
	s_or_b64 exec, exec, s[10:11]
	v_mov_b32_e32 v1, 0x2000
	v_mov_b32_e32 v2, 1
	s_waitcnt vmcnt(0)
	buffer_inv sc1
	s_waitcnt vmcnt(0)
	s_branch .LBB0_1228
.Lvfill0:
	s_or_b64 exec, exec, s[6:7]
	v_readfirstlane_b32 s8, v0
	v_and_b32_e32 v1, 63, v0
	s_lshr_b32 s8, s8, 6
	v_lshlrev_b32_e32 v1, 4, v1
	s_lshl_b32 s9, s2, 17
	s_add_u32 s10, s90, 0x13a00000
	s_addc_u32 s11, s91, 0
	s_add_u32 s10, s10, s9
	s_addc_u32 s11, s11, 0
	s_lshl_b32 s9, s8, 10
	s_mov_b32 s14, 0
.Lvfill0_a:
	s_add_u32 s15, s9, s14
	s_mov_b32 m0, s15
	s_add_u32 s12, s10, s15
	s_addc_u32 s13, s11, 0
	global_load_lds_dwordx4 v1, s[12:13]
	s_add_u32 s14, s14, 0x2000
	s_cmp_lt_u32 s14, 0x20000
	s_cbranch_scc1 .Lvfill0_a
	s_add_i32 s14, s8, -1
.Lvfill0_b:
	s_lshl_b32 s15, s14, 13
	s_mov_b32 m0, s15
	s_add_u32 s12, s10, s15
	s_addc_u32 s13, s11, 0
	global_load_lds_dwordx4 v1, s[12:13]
	s_add_i32 s14, s14, 7
	s_cmp_lt_u32 s14, 16
	s_cbranch_scc1 .Lvfill0_b

; #define LAS __attribute__((address_space(3)))
; template <bool RUN_L = true, bool RUN_G = true, bool DRY = false>
; __device__ __forceinline__ void phase_vaccH(unsigned char* ws, LAS unsigned char* lds, int layer, int G) {
;     ...
;     for (int cg = blockIdx.x; cg < NGRP; cg += G) {
;         __syncthreads();
;         { const u32x4* src = (const u32x4*)(pvl + (size_t)cg * (NEXP * 8)) + tid; u32x4 t_[16];
; #pragma unroll
;           for (int i = 0; i < 16; ++i) t_[i] = src[512 * i];
; #pragma unroll
;           for (int i = 0; i < 16; ++i) ((LAS u32x4*)lds)[tid + 512 * i] = t_[i]; }
;         __syncthreads();
;         if (wid < 4) { if (RUN_L) {
.LBB0_1231:
	s_ashr_i32 s29, s28, 31
	s_lshl_b64 s[22:23], s[28:29], 17
	s_waitcnt vmcnt(0)
	v_lshl_add_u64 v[58:59], v[130:131], 0, s[22:23]
	s_waitcnt vmcnt(2)
	v_add_co_u32_e32 v6, vcc, 0x2000, v58
	s_mov_b32 s8, 0x12000
	s_nop 0
	v_addc_co_u32_e32 v7, vcc, 0, v59, vcc
	v_add_co_u32_e32 v10, vcc, 0x4000, v58
	s_waitcnt vmcnt(2)
	s_nop 0
	v_addc_co_u32_e32 v11, vcc, 0, v59, vcc
	v_add_co_u32_e32 v14, vcc, 0x6000, v58
	s_barrier
	s_nop 0
	v_addc_co_u32_e32 v15, vcc, 0, v59, vcc
	v_add_co_u32_e32 v18, vcc, 0x8000, v58
	s_nop 1
	v_addc_co_u32_e32 v19, vcc, 0, v59, vcc
	v_add_co_u32_e32 v22, vcc, 0xa000, v58
	s_nop 0
	v_addc_co_u32_e32 v23, vcc, 0, v59, vcc
	v_add_co_u32_e32 v26, vcc, 0xc000, v58
	s_nop 0
	v_addc_co_u32_e32 v27, vcc, 0, v59, vcc
	v_add_co_u32_e32 v30, vcc, 0xe000, v58
	s_nop 0
	v_addc_co_u32_e32 v31, vcc, 0, v59, vcc
	v_add_co_u32_e32 v34, vcc, s56, v58
	s_nop 0
	v_addc_co_u32_e32 v35, vcc, 0, v59, vcc
	v_add_co_u32_e32 v38, vcc, s8, v58
	s_mov_b32 s8, 0x14000
	s_nop 0
	v_addc_co_u32_e32 v39, vcc, 0, v59, vcc
	v_add_co_u32_e32 v42, vcc, s8, v58
	s_mov_b32 s8, 0x16000
	s_nop 0
	v_addc_co_u32_e32 v43, vcc, 0, v59, vcc
	v_add_co_u32_e32 v46, vcc, s8, v58
	s_mov_b32 s8, 0x1a000
	s_nop 0
	v_addc_co_u32_e32 v47, vcc, 0, v59, vcc
	s_waitcnt vmcnt(9)
	v_add_co_u32_e32 v50, vcc, s57, v58
	s_nop 0
	s_waitcnt vmcnt(10)
	v_addc_co_u32_e32 v51, vcc, 0, v59, vcc
	v_add_co_u32_e32 v54, vcc, s8, v58
	s_mov_b32 s8, 0x1c000
	s_nop 0
	v_addc_co_u32_e32 v55, vcc, 0, v59, vcc
	v_add_co_u32_e32 v60, vcc, s8, v58
	s_nop 0
	v_addc_co_u32_e32 v61, vcc, 0, v59, vcc
	v_add_co_u32_e32 v62, vcc, s58, v58
	s_nop 0
	v_addc_co_u32_e32 v63, vcc, 0, v59, vcc
	s_nop 0
	s_mov_b64 s[30:31], -1
	s_and_b64 vcc, exec, s[10:11]
	s_waitcnt vmcnt(15)
	s_waitcnt vmcnt(14)
	s_waitcnt vmcnt(13)
	s_waitcnt vmcnt(12)
	s_waitcnt vmcnt(11)
	s_waitcnt vmcnt(10)
	s_waitcnt vmcnt(9)
	s_waitcnt vmcnt(8)
	s_waitcnt vmcnt(7)
	s_waitcnt vmcnt(6)
	s_waitcnt vmcnt(5)
	s_waitcnt vmcnt(4)
	s_waitcnt vmcnt(3)
	s_waitcnt vmcnt(2)
	s_waitcnt vmcnt(1)
	s_waitcnt vmcnt(0)
	s_waitcnt lgkmcnt(0)
	s_barrier
	s_cbranch_vccz .LBB0_1238
	s_or_b64 s[6:7], s[12:13], s[6:7]
	s_and_b64 vcc, exec, s[6:7]
	s_cbranch_vccnz .LBB0_1237
; #define VD_IDS(pw, IT) do { const int t_ = (IT) - ((IT) / MROWS) * MROWS; const unsigned* wp_ = WLP + (size_t)t_ * 128 + r8 * 16 + (lane & 3); \
;         pw[0] = wp_[0]; pw[1] = wp_[4]; pw[2] = wp_[8]; pw[3] = wp_[12]; } while (0)
; #define VD_IDS(pw, IT) do { const int t_ = (IT) - ((IT) / MROWS) * MROWS; const unsigned* wp_ = WLP + (size_t)t_ * 128 + r8 * 16 + (lane & 3); \
;         pw[0] = wp_[0]; pw[1] = wp_[4]; pw[2] = wp_[8]; pw[3] = wp_[12]; } while (0)
; template <bool RUN_L = true, bool RUN_G = true, bool DRY = false>
; __device__ __forceinline__ void phase_vaccH(unsigned char* ws, LAS unsigned char* lds, int layer, int G) {
;     ...
;             if (g < NIT) {
;                 u32x4 ra[16], rc[16]; unsigned pka[16], pkc[16]; f32x2 hva, hvc; f32x2* hpa; f32x2* hpc;
;                 unsigned pw0[4], pw1[4];
;                 VD_IDS(pw0, g);
;                 { const int i1c = g + NG < NIT ? g + NG : g; VD_IDS(pw1, i1c); }
;                 VD_ISSUE(ra, pka, hva, hpa, pw0, g);
	global_load_dword v2, v[136:137], off
	global_load_dword v3, v[136:137], off offset:16
	global_load_dword v4, v[136:137], off offset:32
	global_load_dword v5, v[136:137], off offset:48
	global_load_dword v191, v[138:139], off offset:48
	global_load_dword v193, v[138:139], off offset:32
	global_load_dword v194, v[138:139], off offset:16
	global_load_dword v195, v[138:139], off
	v_mov_b64_e32 v[156:157], v[142:143]
	s_mov_b32 s6, s35
	s_waitcnt vmcnt(7)
	v_mov_b32_dpp v187, v2 quad_perm:[0,0,0,0] row_mask:0xf bank_mask:0xf bound_ctrl:1
	v_mov_b32_dpp v186, v2 quad_perm:[1,1,1,1] row_mask:0xf bank_mask:0xf bound_ctrl:1
	v_mov_b32_dpp v185, v2 quad_perm:[2,2,2,2] row_mask:0xf bank_mask:0xf bound_ctrl:1
	s_waitcnt vmcnt(4)
	v_mov_b32_dpp v172, v5 quad_perm:[3,3,3,3] row_mask:0xf bank_mask:0xf bound_ctrl:1
	v_mov_b32_dpp v173, v5 quad_perm:[2,2,2,2] row_mask:0xf bank_mask:0xf bound_ctrl:1
	v_lshlrev_b32_sdwa v132, v168, v172 dst_sel:DWORD dst_unused:UNUSED_PAD src0_sel:DWORD src1_sel:WORD_1
	v_mov_b32_dpp v184, v2 quad_perm:[3,3,3,3] row_mask:0xf bank_mask:0xf bound_ctrl:1
	v_mov_b32_dpp v183, v3 quad_perm:[0,0,0,0] row_mask:0xf bank_mask:0xf bound_ctrl:1
	v_mov_b32_dpp v182, v3 quad_perm:[1,1,1,1] row_mask:0xf bank_mask:0xf bound_ctrl:1
	v_mov_b32_dpp v181, v3 quad_perm:[2,2,2,2] row_mask:0xf bank_mask:0xf bound_ctrl:1
	v_mov_b32_dpp v180, v3 quad_perm:[3,3,3,3] row_mask:0xf bank_mask:0xf bound_ctrl:1
	v_mov_b32_dpp v174, v5 quad_perm:[1,1,1,1] row_mask:0xf bank_mask:0xf bound_ctrl:1
	v_lshl_add_u64 v[2:3], v[140:141], 0, v[132:133]
	v_lshlrev_b32_sdwa v132, v168, v173 dst_sel:DWORD dst_unused:UNUSED_PAD src0_sel:DWORD src1_sel:WORD_1
	v_mov_b32_dpp v175, v5 quad_perm:[0,0,0,0] row_mask:0xf bank_mask:0xf bound_ctrl:1
	v_lshl_add_u64 v[6:7], v[140:141], 0, v[132:133]
	v_lshlrev_b32_sdwa v132, v168, v174 dst_sel:DWORD dst_unused:UNUSED_PAD src0_sel:DWORD src1_sel:WORD_1
	v_mov_b32_dpp v176, v4 quad_perm:[3,3,3,3] row_mask:0xf bank_mask:0xf bound_ctrl:1
	v_lshl_add_u64 v[10:11], v[140:141], 0, v[132:133]
	v_lshlrev_b32_sdwa v132, v168, v175 dst_sel:DWORD dst_unused:UNUSED_PAD src0_sel:DWORD src1_sel:WORD_1
	v_mov_b32_dpp v177, v4 quad_perm:[2,2,2,2] row_mask:0xf bank_mask:0xf bound_ctrl:1
	v_lshl_add_u64 v[14:15], v[140:141], 0, v[132:133]
	v_lshlrev_b32_sdwa v132, v168, v176 dst_sel:DWORD dst_unused:UNUSED_PAD src0_sel:DWORD src1_sel:WORD_1
	v_mov_b32_dpp v178, v4 quad_perm:[1,1,1,1] row_mask:0xf bank_mask:0xf bound_ctrl:1
	v_lshl_add_u64 v[18:19], v[140:141], 0, v[132:133]
	v_lshlrev_b32_sdwa v132, v168, v177 dst_sel:DWORD dst_unused:UNUSED_PAD src0_sel:DWORD src1_sel:WORD_1
	v_mov_b32_dpp v179, v4 quad_perm:[0,0,0,0] row_mask:0xf bank_mask:0xf bound_ctrl:1
	v_lshl_add_u64 v[22:23], v[140:141], 0, v[132:133]
	v_lshlrev_b32_sdwa v132, v168, v178 dst_sel:DWORD dst_unused:UNUSED_PAD src0_sel:DWORD src1_sel:WORD_1
	v_lshl_add_u64 v[26:27], v[140:141], 0, v[132:133]
	v_lshlrev_b32_sdwa v132, v168, v179 dst_sel:DWORD dst_unused:UNUSED_PAD src0_sel:DWORD src1_sel:WORD_1
	v_lshl_add_u64 v[30:31], v[140:141], 0, v[132:133]
	v_lshlrev_b32_sdwa v132, v168, v180 dst_sel:DWORD dst_unused:UNUSED_PAD src0_sel:DWORD src1_sel:WORD_1
	v_lshl_add_u64 v[34:35], v[140:141], 0, v[132:133]
	v_lshlrev_b32_sdwa v132, v168, v181 dst_sel:DWORD dst_unused:UNUSED_PAD src0_sel:DWORD src1_sel:WORD_1
	v_lshl_add_u64 v[38:39], v[140:141], 0, v[132:133]
	v_lshlrev_b32_sdwa v132, v168, v182 dst_sel:DWORD dst_unused:UNUSED_PAD src0_sel:DWORD src1_sel:WORD_1
	v_lshl_add_u64 v[42:43], v[140:141], 0, v[132:133]
	v_lshlrev_b32_sdwa v132, v168, v183 dst_sel:DWORD dst_unused:UNUSED_PAD src0_sel:DWORD src1_sel:WORD_1
	v_lshl_add_u64 v[46:47], v[140:141], 0, v[132:133]
	v_lshlrev_b32_sdwa v132, v168, v184 dst_sel:DWORD dst_unused:UNUSED_PAD src0_sel:DWORD src1_sel:WORD_1
	v_lshl_add_u64 v[50:51], v[140:141], 0, v[132:133]
	v_lshlrev_b32_sdwa v132, v168, v185 dst_sel:DWORD dst_unused:UNUSED_PAD src0_sel:DWORD src1_sel:WORD_1
	v_lshl_add_u64 v[54:55], v[140:141], 0, v[132:133]
	v_lshlrev_b32_sdwa v132, v168, v186 dst_sel:DWORD dst_unused:UNUSED_PAD src0_sel:DWORD src1_sel:WORD_1
	v_lshl_add_u64 v[58:59], v[140:141], 0, v[132:133]
	v_lshlrev_b32_sdwa v132, v168, v187 dst_sel:DWORD dst_unused:UNUSED_PAD src0_sel:DWORD src1_sel:WORD_1
	v_lshl_add_u64 v[62:63], v[140:141], 0, v[132:133]
	global_load_dwordx2 v[150:151], v[142:143], off
	s_nop 0
	global_load_dwordx4 v[2:5], v[2:3], off
	s_nop 0
	global_load_dwordx4 v[6:9], v[6:7], off
	s_nop 0
	global_load_dwordx4 v[10:13], v[10:11], off
	s_nop 0
	global_load_dwordx4 v[14:17], v[14:15], off
	s_nop 0
	global_load_dwordx4 v[18:21], v[18:19], off
	s_nop 0
	global_load_dwordx4 v[22:25], v[22:23], off
	s_nop 0
	global_load_dwordx4 v[26:29], v[26:27], off
	s_nop 0
	global_load_dwordx4 v[30:33], v[30:31], off
	s_nop 0
	global_load_dwordx4 v[34:37], v[34:35], off
	s_nop 0
	global_load_dwordx4 v[38:41], v[38:39], off
	s_nop 0
	global_load_dwordx4 v[42:45], v[42:43], off
	s_nop 0
	global_load_dwordx4 v[46:49], v[46:47], off
	s_nop 0
	global_load_dwordx4 v[50:53], v[50:51], off
	s_nop 0
	global_load_dwordx4 v[54:57], v[54:55], off
	s_nop 0
	global_load_dwordx4 v[58:61], v[58:59], off
	s_nop 0
	global_load_dwordx4 v[62:65], v[62:63], off
	s_branch .LBB0_1235

; #define LAS __attribute__((address_space(3)))
; template <bool RUN_L = true, bool RUN_G = true, bool DRY = false>
; __device__ __forceinline__ void phase_vaccH(unsigned char* ws, LAS unsigned char* lds, int layer, int G) {
;     ...
;         { const u32x4* src = (const u32x4*)(pvl + (size_t)cg * (NEXP * 8)) + tid; u32x4 t_[16];
; #pragma unroll
;           for (int i = 0; i < 16; ++i) t_[i] = src[512 * i];
; #pragma unroll
;           for (int i = 0; i < 16; ++i) ((LAS u32x4*)lds)[tid + 512 * i] = t_[i]; }
.Lvfill1:
	s_or_b64 exec, exec, s[6:7]
	v_readfirstlane_b32 s8, v0
	v_and_b32_e32 v1, 63, v0
	s_lshr_b32 s8, s8, 6
	v_lshlrev_b32_e32 v1, 4, v1
	s_lshl_b32 s9, s2, 17
	s_add_u32 s10, s90, 0x17a00000
	s_addc_u32 s11, s91, 0
	s_add_u32 s10, s10, s9
	s_addc_u32 s11, s11, 0
	s_lshl_b32 s9, s8, 10
	s_mov_b32 s14, 0

; #define LAS __attribute__((address_space(3)))
; template <bool RUN_L = true, bool RUN_G = true, bool DRY = false>
; __device__ __forceinline__ void phase_vaccH(unsigned char* ws, LAS unsigned char* lds, int layer, int G) {
;     ...
;     for (int cg = blockIdx.x; cg < NGRP; cg += G) {
;         __syncthreads();
;         { const u32x4* src = (const u32x4*)(pvl + (size_t)cg * (NEXP * 8)) + tid; u32x4 t_[16];
; #pragma unroll
;           for (int i = 0; i < 16; ++i) t_[i] = src[512 * i];
; #pragma unroll
;           for (int i = 0; i < 16; ++i) ((LAS u32x4*)lds)[tid + 512 * i] = t_[i]; }
;         __syncthreads();
;         if (wid < 4) { if (RUN_L) {
.LBB0_1976:
	s_ashr_i32 s23, s22, 31
	s_lshl_b64 s[24:25], s[22:23], 17
	s_waitcnt vmcnt(0)
	v_lshl_add_u64 v[58:59], v[130:131], 0, s[24:25]
	s_waitcnt vmcnt(2)
	v_add_co_u32_e32 v6, vcc, 0x2000, v58
	s_nop 1
	v_addc_co_u32_e32 v7, vcc, 0, v59, vcc
	v_add_co_u32_e32 v10, vcc, 0x4000, v58
	s_barrier
	s_waitcnt vmcnt(2)
	v_addc_co_u32_e32 v11, vcc, 0, v59, vcc
	v_add_co_u32_e32 v14, vcc, 0x6000, v58
	s_nop 1
	v_addc_co_u32_e32 v15, vcc, 0, v59, vcc
	v_add_co_u32_e32 v18, vcc, 0x8000, v58
	s_nop 0
	v_addc_co_u32_e32 v19, vcc, 0, v59, vcc
	v_add_co_u32_e32 v22, vcc, 0xa000, v58
	s_nop 0
	v_addc_co_u32_e32 v23, vcc, 0, v59, vcc
	v_add_co_u32_e32 v26, vcc, 0xc000, v58
	s_nop 0
	v_addc_co_u32_e32 v27, vcc, 0, v59, vcc
	v_add_co_u32_e32 v30, vcc, 0xe000, v58
	s_mov_b64 s[28:29], -1
	s_nop 0
	v_addc_co_u32_e32 v31, vcc, 0, v59, vcc
	v_add_co_u32_e32 v34, vcc, s41, v58
	s_nop 0
	v_addc_co_u32_e32 v35, vcc, 0, v59, vcc
	v_add_co_u32_e32 v38, vcc, s42, v58
	s_nop 1
	v_addc_co_u32_e32 v39, vcc, 0, v59, vcc
	v_add_co_u32_e32 v42, vcc, s43, v58
	s_nop 0
	s_waitcnt vmcnt(11)
	v_addc_co_u32_e32 v43, vcc, 0, v59, vcc
	v_add_co_u32_e32 v46, vcc, s44, v58
	s_nop 1
	v_addc_co_u32_e32 v47, vcc, 0, v59, vcc
	v_add_co_u32_e32 v50, vcc, s45, v58
	s_nop 0
	v_addc_co_u32_e32 v51, vcc, 0, v59, vcc
	v_add_co_u32_e32 v54, vcc, s46, v58
	s_nop 1
	v_addc_co_u32_e32 v55, vcc, 0, v59, vcc
	v_add_co_u32_e32 v60, vcc, s47, v58
	s_nop 0
	v_addc_co_u32_e32 v61, vcc, 0, v59, vcc
	v_add_co_u32_e32 v62, vcc, s48, v58
	s_nop 1
	v_addc_co_u32_e32 v63, vcc, 0, v59, vcc
	s_nop 0
	s_and_b64 vcc, exec, s[10:11]
	s_waitcnt vmcnt(15)
	s_waitcnt vmcnt(14)
	s_waitcnt vmcnt(13)
	s_waitcnt vmcnt(12)
	s_waitcnt vmcnt(11)
	s_waitcnt vmcnt(10)
	s_waitcnt vmcnt(9)
	s_waitcnt vmcnt(8)
	s_waitcnt vmcnt(7)
	s_waitcnt vmcnt(6)
	s_waitcnt vmcnt(5)
	s_waitcnt vmcnt(4)
	s_waitcnt vmcnt(3)
	s_waitcnt vmcnt(2)
	s_waitcnt vmcnt(1)
	s_waitcnt vmcnt(0)
	s_waitcnt lgkmcnt(0)
	s_barrier
	s_cbranch_vccz .LBB0_1983
	s_or_b64 s[6:7], s[12:13], s[6:7]
	s_and_b64 vcc, exec, s[6:7]
	s_cbranch_vccnz .LBB0_1982
; #define VD_IDS(pw, IT) do { const int t_ = (IT) - ((IT) / MROWS) * MROWS; const unsigned* wp_ = WLP + (size_t)t_ * 128 + r8 * 16 + (lane & 3); \
;         pw[0] = wp_[0]; pw[1] = wp_[4]; pw[2] = wp_[8]; pw[3] = wp_[12]; } while (0)
; #define VD_IDS(pw, IT) do { const int t_ = (IT) - ((IT) / MROWS) * MROWS; const unsigned* wp_ = WLP + (size_t)t_ * 128 + r8 * 16 + (lane & 3); \
;         pw[0] = wp_[0]; pw[1] = wp_[4]; pw[2] = wp_[8]; pw[3] = wp_[12]; } while (0)
; template <bool RUN_L = true, bool RUN_G = true, bool DRY = false>
; __device__ __forceinline__ void phase_vaccH(unsigned char* ws, LAS unsigned char* lds, int layer, int G) {
;     ...
;             if (g < NIT) {
;                 u32x4 ra[16], rc[16]; unsigned pka[16], pkc[16]; f32x2 hva, hvc; f32x2* hpa; f32x2* hpc;
;                 unsigned pw0[4], pw1[4];
;                 VD_IDS(pw0, g);
;                 { const int i1c = g + NG < NIT ? g + NG : g; VD_IDS(pw1, i1c); }
;                 VD_ISSUE(ra, pka, hva, hpa, pw0, g);
	global_load_dword v2, v[136:137], off
	global_load_dword v3, v[136:137], off offset:16
	global_load_dword v4, v[136:137], off offset:32
	global_load_dword v5, v[136:137], off offset:48
	global_load_dword v191, v[138:139], off offset:48
	global_load_dword v193, v[138:139], off offset:32
	global_load_dword v194, v[138:139], off offset:16
	global_load_dword v195, v[138:139], off
	v_mov_b64_e32 v[156:157], v[142:143]
	s_mov_b32 s6, s35
	s_waitcnt vmcnt(7)
	v_mov_b32_dpp v187, v2 quad_perm:[0,0,0,0] row_mask:0xf bank_mask:0xf bound_ctrl:1
	v_mov_b32_dpp v186, v2 quad_perm:[1,1,1,1] row_mask:0xf bank_mask:0xf bound_ctrl:1
	v_mov_b32_dpp v185, v2 quad_perm:[2,2,2,2] row_mask:0xf bank_mask:0xf bound_ctrl:1
	s_waitcnt vmcnt(4)
	v_mov_b32_dpp v172, v5 quad_perm:[3,3,3,3] row_mask:0xf bank_mask:0xf bound_ctrl:1
	v_mov_b32_dpp v173, v5 quad_perm:[2,2,2,2] row_mask:0xf bank_mask:0xf bound_ctrl:1
	v_lshlrev_b32_sdwa v132, v168, v172 dst_sel:DWORD dst_unused:UNUSED_PAD src0_sel:DWORD src1_sel:WORD_1
	v_mov_b32_dpp v184, v2 quad_perm:[3,3,3,3] row_mask:0xf bank_mask:0xf bound_ctrl:1
	v_mov_b32_dpp v183, v3 quad_perm:[0,0,0,0] row_mask:0xf bank_mask:0xf bound_ctrl:1
	v_mov_b32_dpp v182, v3 quad_perm:[1,1,1,1] row_mask:0xf bank_mask:0xf bound_ctrl:1
	v_mov_b32_dpp v181, v3 quad_perm:[2,2,2,2] row_mask:0xf bank_mask:0xf bound_ctrl:1
	v_mov_b32_dpp v180, v3 quad_perm:[3,3,3,3] row_mask:0xf bank_mask:0xf bound_ctrl:1
	v_mov_b32_dpp v174, v5 quad_perm:[1,1,1,1] row_mask:0xf bank_mask:0xf bound_ctrl:1
	v_lshl_add_u64 v[2:3], v[140:141], 0, v[132:133]
	v_lshlrev_b32_sdwa v132, v168, v173 dst_sel:DWORD dst_unused:UNUSED_PAD src0_sel:DWORD src1_sel:WORD_1
	v_mov_b32_dpp v175, v5 quad_perm:[0,0,0,0] row_mask:0xf bank_mask:0xf bound_ctrl:1
	v_lshl_add_u64 v[6:7], v[140:141], 0, v[132:133]
	v_lshlrev_b32_sdwa v132, v168, v174 dst_sel:DWORD dst_unused:UNUSED_PAD src0_sel:DWORD src1_sel:WORD_1
	v_mov_b32_dpp v176, v4 quad_perm:[3,3,3,3] row_mask:0xf bank_mask:0xf bound_ctrl:1
	v_lshl_add_u64 v[10:11], v[140:141], 0, v[132:133]
	v_lshlrev_b32_sdwa v132, v168, v175 dst_sel:DWORD dst_unused:UNUSED_PAD src0_sel:DWORD src1_sel:WORD_1
	v_mov_b32_dpp v177, v4 quad_perm:[2,2,2,2] row_mask:0xf bank_mask:0xf bound_ctrl:1
	v_lshl_add_u64 v[14:15], v[140:141], 0, v[132:133]
	v_lshlrev_b32_sdwa v132, v168, v176 dst_sel:DWORD dst_unused:UNUSED_PAD src0_sel:DWORD src1_sel:WORD_1
	v_mov_b32_dpp v178, v4 quad_perm:[1,1,1,1] row_mask:0xf bank_mask:0xf bound_ctrl:1
	v_lshl_add_u64 v[18:19], v[140:141], 0, v[132:133]
	v_lshlrev_b32_sdwa v132, v168, v177 dst_sel:DWORD dst_unused:UNUSED_PAD src0_sel:DWORD src1_sel:WORD_1
	v_mov_b32_dpp v179, v4 quad_perm:[0,0,0,0] row_mask:0xf bank_mask:0xf bound_ctrl:1
	v_lshl_add_u64 v[22:23], v[140:141], 0, v[132:133]
	v_lshlrev_b32_sdwa v132, v168, v178 dst_sel:DWORD dst_unused:UNUSED_PAD src0_sel:DWORD src1_sel:WORD_1
	v_lshl_add_u64 v[26:27], v[140:141], 0, v[132:133]
	v_lshlrev_b32_sdwa v132, v168, v179 dst_sel:DWORD dst_unused:UNUSED_PAD src0_sel:DWORD src1_sel:WORD_1
	v_lshl_add_u64 v[30:31], v[140:141], 0, v[132:133]
	v_lshlrev_b32_sdwa v132, v168, v180 dst_sel:DWORD dst_unused:UNUSED_PAD src0_sel:DWORD src1_sel:WORD_1
	v_lshl_add_u64 v[34:35], v[140:141], 0, v[132:133]
	v_lshlrev_b32_sdwa v132, v168, v181 dst_sel:DWORD dst_unused:UNUSED_PAD src0_sel:DWORD src1_sel:WORD_1
	v_lshl_add_u64 v[38:39], v[140:141], 0, v[132:133]
	v_lshlrev_b32_sdwa v132, v168, v182 dst_sel:DWORD dst_unused:UNUSED_PAD src0_sel:DWORD src1_sel:WORD_1
	v_lshl_add_u64 v[42:43], v[140:141], 0, v[132:133]
	v_lshlrev_b32_sdwa v132, v168, v183 dst_sel:DWORD dst_unused:UNUSED_PAD src0_sel:DWORD src1_sel:WORD_1
	v_lshl_add_u64 v[46:47], v[140:141], 0, v[132:133]
	v_lshlrev_b32_sdwa v132, v168, v184 dst_sel:DWORD dst_unused:UNUSED_PAD src0_sel:DWORD src1_sel:WORD_1
	v_lshl_add_u64 v[50:51], v[140:141], 0, v[132:133]
	v_lshlrev_b32_sdwa v132, v168, v185 dst_sel:DWORD dst_unused:UNUSED_PAD src0_sel:DWORD src1_sel:WORD_1
	v_lshl_add_u64 v[54:55], v[140:141], 0, v[132:133]
	v_lshlrev_b32_sdwa v132, v168, v186 dst_sel:DWORD dst_unused:UNUSED_PAD src0_sel:DWORD src1_sel:WORD_1
	v_lshl_add_u64 v[58:59], v[140:141], 0, v[132:133]
	v_lshlrev_b32_sdwa v132, v168, v187 dst_sel:DWORD dst_unused:UNUSED_PAD src0_sel:DWORD src1_sel:WORD_1
	v_lshl_add_u64 v[62:63], v[140:141], 0, v[132:133]
	global_load_dwordx2 v[150:151], v[142:143], off
	s_nop 0
	global_load_dwordx4 v[2:5], v[2:3], off
	s_nop 0
	global_load_dwordx4 v[6:9], v[6:7], off
	s_nop 0
	global_load_dwordx4 v[10:13], v[10:11], off
	s_nop 0
	global_load_dwordx4 v[14:17], v[14:15], off
	s_nop 0
	global_load_dwordx4 v[18:21], v[18:19], off
	s_nop 0
	global_load_dwordx4 v[22:25], v[22:23], off
	s_nop 0
	global_load_dwordx4 v[26:29], v[26:27], off
	s_nop 0
	global_load_dwordx4 v[30:33], v[30:31], off
	s_nop 0
	global_load_dwordx4 v[34:37], v[34:35], off
	s_nop 0
	global_load_dwordx4 v[38:41], v[38:39], off
	s_nop 0
	global_load_dwordx4 v[42:45], v[42:43], off
	s_nop 0
	global_load_dwordx4 v[46:49], v[46:47], off
	s_nop 0
	global_load_dwordx4 v[50:53], v[50:51], off
	s_nop 0
	global_load_dwordx4 v[54:57], v[54:55], off
	s_nop 0
	global_load_dwordx4 v[58:61], v[58:59], off
	s_nop 0
	global_load_dwordx4 v[62:65], v[62:63], off
	s_branch .LBB0_1980
